# v048 + bundle of exact reorderings: P13 loop edge straightened, K-fragment and mask reads behind the barrier, first-half row sums in the MFMA wait, P11 reads before the DMA piece, P3 ballot trimmed
# speedup vs baseline: 1.0054x; 1.0054x over previous
.LBB0_269:
	v_pk_add_f32 v[114:115], v[98:99], 0 op_sel_hi:[1,0]
	v_max_i32_e32 v116, 0, v82
	v_pk_add_f32 v[114:115], v[100:101], v[114:115]
	v_max_i32_e32 v117, 0, v83
	v_pk_add_f32 v[114:115], v[102:103], v[114:115]
	v_max_i32_e32 v118, 0, v84
	v_pk_add_f32 v[114:115], v[104:105], v[114:115]
	v_max_i32_e32 v119, 0, v85
	v_pk_add_f32 v[114:115], v[106:107], v[114:115]
	v_max_i32_e32 v120, 0, v86
	v_pk_add_f32 v[114:115], v[108:109], v[114:115]
	v_max_i32_e32 v121, 0, v87
	v_pk_add_f32 v[114:115], v[110:111], v[114:115]
	v_max_i32_e32 v122, 0, v88
	v_pk_add_f32 v[114:115], v[112:113], v[114:115]
	v_max_i32_e32 v123, 0, v89
	v_pk_add_f32 v[204:205], v[114:115], v[114:115] op_sel:[0,1] op_sel_hi:[1,0]
	v_exp_f32_e64 v114, -|v82|
	v_exp_f32_e64 v115, -|v83|
	v_max_i32_e32 v124, 0, v90
	v_max_i32_e32 v125, 0, v91
	v_max_i32_e32 v126, 0, v92
	v_pk_add_f32 v[114:115], v[114:115], 1.0 op_sel_hi:[1,0]
	v_max_i32_e32 v127, 0, v93
	v_log_f32_e32 v114, v114
	v_log_f32_e32 v115, v115
	v_max_i32_e32 v128, 0, v94
	v_max_i32_e32 v129, 0, v95
	v_max_i32_e32 v208, 0, v96
	v_pk_add_f32 v[114:115], v[114:115], v[116:117]
	v_exp_f32_e64 v116, -|v84|
	v_exp_f32_e64 v117, -|v85|
	v_max_i32_e32 v209, 0, v97
	v_sub_f32_e32 v225, v203, v115
	v_sub_f32_e32 v224, v203, v114
	v_pk_add_f32 v[116:117], v[116:117], 1.0 op_sel_hi:[1,0]
	v_cvt_pk_bf16_f32 v98, v98, v99
	v_log_f32_e32 v116, v116
	v_log_f32_e32 v117, v117
	v_cvt_pk_bf16_f32 v99, v100, v101
	v_cvt_pk_bf16_f32 v100, v102, v103
	v_cvt_pk_bf16_f32 v101, v104, v105
	v_pk_add_f32 v[116:117], v[116:117], v[118:119]
	v_exp_f32_e64 v118, -|v86|
	v_exp_f32_e64 v119, -|v87|
	v_sub_f32_e32 v227, v203, v117
	v_sub_f32_e32 v226, v203, v116
	v_pk_add_f32 v[84:85], v[84:85], v[226:227]
	v_pk_add_f32 v[118:119], v[118:119], 1.0 op_sel_hi:[1,0]
	v_pk_add_f32 v[82:83], v[82:83], v[224:225]
	v_log_f32_e32 v118, v118
	v_log_f32_e32 v119, v119
	v_mfma_f32_32x32x16_bf16 v[66:81], v[130:133], v[98:101], v[66:81]
	v_cvt_pk_bf16_f32 v98, v114, v115
	v_cvt_pk_bf16_f32 v99, v116, v117
	v_add_f32_e64 v118, v118, v120
	v_add_f32_e64 v119, v119, v121
	v_exp_f32_e64 v120, -|v88|
	v_exp_f32_e64 v121, -|v89|
	v_sub_f32_e32 v229, v203, v119
	v_sub_f32_e32 v228, v203, v118
	v_pk_add_f32 v[86:87], v[86:87], v[228:229]
	v_pk_add_f32 v[120:121], v[120:121], 1.0 op_sel_hi:[1,0]
	v_cvt_pk_bf16_f32 v100, v118, v119
	v_log_f32_e32 v120, v120
	v_log_f32_e32 v121, v121
	v_add_u32_e32 v244, s81, v210
	v_mov_b32_e32 v206, v204
	s_nop 1
	v_permlane32_swap_b32_e32 v204, v206
	v_pk_add_f32 v[122:123], v[120:121], v[122:123]
	v_exp_f32_e64 v120, -|v90|
	v_exp_f32_e64 v121, -|v91|
	v_sub_f32_e32 v231, v203, v123
	v_sub_f32_e32 v230, v203, v122
	v_pk_add_f32 v[88:89], v[88:89], v[230:231]
	v_pk_add_f32 v[120:121], v[120:121], 1.0 op_sel_hi:[1,0]
	v_cvt_pk_bf16_f32 v101, v122, v123
	v_log_f32_e32 v120, v120
	v_log_f32_e32 v121, v121
	s_nop 0
	v_pk_add_f32 v[120:121], v[120:121], v[124:125]
	v_exp_f32_e64 v124, -|v92|
	v_exp_f32_e64 v125, -|v93|
	v_sub_f32_e32 v233, v203, v121
	v_sub_f32_e32 v232, v203, v120
	v_pk_add_f32 v[90:91], v[90:91], v[232:233]
	v_pk_add_f32 v[124:125], v[124:125], 1.0 op_sel_hi:[1,0]
	s_nop 0
	v_log_f32_e32 v124, v124
	v_log_f32_e32 v125, v125
	s_nop 0
	v_pk_add_f32 v[124:125], v[124:125], v[126:127]
	v_exp_f32_e64 v126, -|v94|
	v_exp_f32_e64 v127, -|v95|
	v_sub_f32_e32 v235, v203, v125
	v_sub_f32_e32 v234, v203, v124
	v_pk_add_f32 v[92:93], v[92:93], v[234:235]
	v_pk_add_f32 v[126:127], v[126:127], 1.0 op_sel_hi:[1,0]
	s_nop 0
	v_log_f32_e32 v126, v126
	v_log_f32_e32 v127, v127
	s_nop 0
	v_pk_add_f32 v[126:127], v[126:127], v[128:129]
	v_exp_f32_e64 v128, -|v96|
	v_exp_f32_e64 v129, -|v97|
	v_sub_f32_e32 v237, v203, v127
	v_sub_f32_e32 v236, v203, v126
	v_pk_add_f32 v[94:95], v[94:95], v[236:237]
	v_pk_add_f32 v[128:129], v[128:129], 1.0 op_sel_hi:[1,0]
	s_nop 0
	v_log_f32_e32 v128, v128
	v_log_f32_e32 v129, v129
	s_nop 0
	v_pk_add_f32 v[128:129], v[128:129], v[208:209]
	s_nop 0
	v_sub_f32_e32 v239, v203, v129
	v_sub_f32_e32 v238, v203, v128
	v_pk_add_f32 v[96:97], v[96:97], v[238:239]
	v_pk_add_f32 v[208:209], v[114:115], v[116:117]
	s_nop 0
	v_mfma_f32_32x32x16_bf16 v[82:97], v[130:133], v[98:101], v[82:97]
	v_cvt_pk_bf16_f32 v98, v106, v107
	v_cvt_pk_bf16_f32 v99, v108, v109
	v_cvt_pk_bf16_f32 v100, v110, v111
	v_cvt_pk_bf16_f32 v101, v112, v113
	v_add_f32_e64 v208, v118, v208
	v_add_f32_e64 v209, v119, v209
	v_pk_add_f32 v[208:209], v[122:123], v[208:209]
	v_mfma_f32_32x32x16_bf16 v[66:81], v[134:137], v[98:101], v[66:81]
	v_cvt_pk_bf16_f32 v98, v120, v121
	v_cvt_pk_bf16_f32 v99, v124, v125
	v_cvt_pk_bf16_f32 v100, v126, v127
	v_cvt_pk_bf16_f32 v101, v128, v129
	v_add_f32_e64 v208, v120, v208
	v_add_f32_e64 v209, v121, v209
	s_nop 5
	v_exp_f32_e32 v66, v66
	v_mfma_f32_32x32x16_bf16 v[82:97], v[134:137], v[98:101], v[82:97]
	v_add_f32_e64 v208, v124, v208
	v_add_f32_e64 v209, v125, v209
	v_exp_f32_e32 v67, v67
	v_pk_add_f32 v[208:209], v[126:127], v[208:209]
	v_exp_f32_e32 v68, v68
	v_exp_f32_e32 v69, v69
	v_exp_f32_e32 v70, v70
	v_exp_f32_e32 v71, v71
	s_nop 3
	v_exp_f32_e32 v86, v86
	v_exp_f32_e32 v87, v87
	v_exp_f32_e32 v88, v88
	v_exp_f32_e32 v89, v89
	v_exp_f32_e32 v98, v82
	v_exp_f32_e32 v99, v83
	v_exp_f32_e32 v100, v84
	v_exp_f32_e32 v101, v85
	v_exp_f32_e32 v72, v72
	v_exp_f32_e32 v73, v73
	v_cvt_pk_bf16_f32 v226, v86, v87
	v_cvt_pk_bf16_f32 v227, v88, v89
	s_nop 0
	ds_read_b64_tr_b16 v[86:87], v244 offset:4096
	ds_read_b64_tr_b16 v[88:89], v244 offset:5120
	ds_read_b64_tr_b16 v[228:229], v244 offset:4608
	ds_read_b64_tr_b16 v[230:231], v244 offset:5632
	v_pk_add_f32 v[208:209], v[128:129], v[208:209]
	v_exp_f32_e32 v205, v90
	v_exp_f32_e32 v223, v91
	v_pk_add_f32 v[208:209], v[208:209], v[208:209] op_sel:[0,1] op_sel_hi:[1,0]
	v_exp_f32_e32 v232, v76
	v_mov_b32_e32 v207, v208
	s_nop 1
	v_permlane32_swap_b32_e32 v208, v207
	v_exp_f32_e32 v233, v92
	v_exp_f32_e32 v234, v77
	v_exp_f32_e32 v235, v93
	v_exp_f32_e32 v236, v78
	v_exp_f32_e32 v237, v94
	v_exp_f32_e32 v238, v79
	v_exp_f32_e32 v239, v95
	v_cvt_pk_bf16_f32 v82, v66, v67
	v_cvt_pk_bf16_f32 v83, v68, v69
	v_cvt_pk_bf16_f32 v84, v70, v71
	v_cvt_pk_bf16_f32 v85, v72, v73
	v_cvt_pk_bf16_f32 v224, v98, v99
	v_cvt_pk_bf16_f32 v225, v100, v101
	v_exp_f32_e32 v175, v74
	v_exp_f32_e32 v209, v75
	v_exp_f32_e32 v240, v80
	v_exp_f32_e32 v241, v96
	v_exp_f32_e32 v242, v81
	v_exp_f32_e32 v243, v97
	s_waitcnt lgkmcnt(2)
	v_mfma_f32_32x32x16_bf16 v[50:65], v[86:89], v[82:85], v[50:65]
	v_mfma_f32_32x32x16_bf16 v[18:33], v[86:89], v[224:227], v[18:33]
	s_waitcnt lgkmcnt(0)
	v_mfma_f32_32x32x16_bf16 v[34:49], v[228:231], v[82:85], v[34:49]
	v_mfma_f32_32x32x16_bf16 v[2:17], v[228:231], v[224:227], v[2:17]
	v_cvt_pk_bf16_f32 v228, v205, v223
	v_mov_b32_e32 v205, v208
	v_add_f32_e64 v204, v204, v206
	v_add_f32_e64 v205, v205, v207
	v_cvt_pk_bf16_f32 v225, v232, v234
	v_pk_add_f32 v[204:205], v[202:203], v[204:205] neg_lo:[0,1] neg_hi:[0,1]
	v_cvt_pk_bf16_f32 v226, v236, v238
	v_cvt_pk_bf16_f32 v229, v233, v235
	v_cvt_pk_bf16_f32 v230, v237, v239
	ds_read_b64_tr_b16 v[232:233], v244 offset:6144
	ds_read_b64_tr_b16 v[234:235], v244 offset:7168
	ds_read_b64_tr_b16 v[236:237], v244 offset:6656
	ds_read_b64_tr_b16 v[238:239], v244 offset:7680
	v_cmp_gt_f32_e32 vcc, s72, v204
	v_cmp_gt_f32_e64 s[0:1], s72, v205
	s_and_b64 s[0:1], vcc, s[0:1]
	v_cvt_pk_bf16_f32 v224, v175, v209
	v_cvt_pk_bf16_f32 v227, v240, v242
	v_cvt_pk_bf16_f32 v231, v241, v243
	s_cmp_lg_u64 s[0:1], exec
	s_waitcnt lgkmcnt(2)
	v_mfma_f32_32x32x16_bf16 v[50:65], v[232:235], v[224:227], v[50:65]
	s_cselect_b64 s[0:1], -1, 0
	v_mfma_f32_32x32x16_bf16 v[18:33], v[232:235], v[228:231], v[18:33]
	s_waitcnt lgkmcnt(0)
	v_mfma_f32_32x32x16_bf16 v[34:49], v[236:239], v[224:227], v[34:49]
	v_mfma_f32_32x32x16_bf16 v[2:17], v[236:239], v[228:231], v[2:17]
	s_branch .LBB0_271

.LBB0_2751:
	v_add_u32_e32 v179, s39, v151
	v_add_u32_e32 v225, v179, v155
	v_add_u32_e32 v224, v179, v181
	v_add_u32_e32 v223, v179, v219
	s_waitcnt lgkmcnt(0)
	v_lshrrev_b32_e32 v82, v163, v226
	v_bfe_i32 v83, v82, 26, 1
	v_bitop3_b32 v96, v16, s28, v83 bitop3:0xe4
	v_bfe_i32 v83, v82, 25, 1
	v_bitop3_b32 v95, v13, s28, v83 bitop3:0xe4
	v_bfe_i32 v83, v82, 24, 1
	v_bitop3_b32 v94, v14, s28, v83 bitop3:0xe4
	v_bfe_i32 v83, v82, 19, 1
	v_bitop3_b32 v93, v11, s28, v83 bitop3:0xe4
	v_bfe_i32 v83, v82, 18, 1
	v_bitop3_b32 v92, v12, s28, v83 bitop3:0xe4
	v_bfe_i32 v83, v82, 17, 1
	v_add_u32_e32 v226, v179, v153
	v_bitop3_b32 v91, v9, s28, v83 bitop3:0xe4
	v_bfe_i32 v83, v82, 16, 1
	v_bitop3_b32 v90, v10, s28, v83 bitop3:0xe4
	v_bfe_i32 v83, v82, 11, 1
	v_bitop3_b32 v89, v7, s28, v83 bitop3:0xe4
	v_bfe_i32 v83, v82, 10, 1
	v_bitop3_b32 v88, v8, s28, v83 bitop3:0xe4
	v_bfe_i32 v83, v82, 9, 1
	v_bitop3_b32 v87, v5, s28, v83 bitop3:0xe4
	v_bfe_i32 v83, v82, 8, 1
	v_bitop3_b32 v86, v6, s28, v83 bitop3:0xe4
	v_bfe_i32 v83, v82, 3, 1
	v_bfe_i32 v84, v82, 27, 1
	v_bitop3_b32 v85, v3, s28, v83 bitop3:0xe4
	v_bfe_i32 v83, v82, 2, 1
	v_bitop3_b32 v97, v15, s28, v84 bitop3:0xe4
	v_bitop3_b32 v84, v4, s28, v83 bitop3:0xe4
	v_bfe_i32 v83, v82, 1, 1
	v_bfe_i32 v82, v82, 0, 1
	v_bitop3_b32 v83, v1, s28, v83 bitop3:0xe4
	v_bitop3_b32 v82, v2, s28, v82 bitop3:0xe4
	v_add_u32_e32 v179, s39, v17
	s_add_i32 s14, s37, 1
	s_waitcnt lgkmcnt(0)
	v_mfma_f32_32x32x16_bf16 v[98:113], v[186:189], v[114:117], v[82:97]
	s_cmp_lg_u32 s37, 2
	s_cselect_b32 s37, s14, 0
	s_add_u32 s0, s0, 0x4000
	s_addc_u32 s1, s1, 0
	s_add_i32 s38, s38, 1
	s_cmp_eq_u32 s36, s0
	v_add_u32_e32 v146, 8, v146
	v_mfma_f32_32x32x16_bf16 v[82:97], v[186:189], v[130:133], v[82:97]
	ds_read_b128 v[186:189], v225
	s_waitcnt lgkmcnt(0)
	v_mfma_f32_32x32x16_bf16 v[98:113], v[186:189], v[118:121], v[98:113]
	v_mfma_f32_32x32x16_bf16 v[82:97], v[186:189], v[134:137], v[82:97]
	ds_read_b128 v[186:189], v224
	s_waitcnt lgkmcnt(0)
	v_mfma_f32_32x32x16_bf16 v[98:113], v[186:189], v[122:125], v[98:113]
	v_mfma_f32_32x32x16_bf16 v[82:97], v[186:189], v[138:141], v[82:97]
	ds_read_b128 v[186:189], v223
	s_waitcnt lgkmcnt(0)
	v_mfma_f32_32x32x16_bf16 v[98:113], v[186:189], v[126:129], v[98:113]
	v_mfma_f32_32x32x16_bf16 v[82:97], v[186:189], v[142:145], v[82:97]
	s_nop 10
	v_exp_f32_e32 v190, v98
	v_exp_f32_e32 v191, v99
	v_exp_f32_e32 v192, v100
	v_exp_f32_e32 v193, v101
	s_nop 0
	ds_read_b64_tr_b16 v[98:99], v179 offset:49152
	ds_read_b64_tr_b16 v[100:101], v179 offset:50176
	v_exp_f32_e32 v188, v102
	v_exp_f32_e32 v189, v103
	v_exp_f32_e32 v186, v104
	v_exp_f32_e32 v187, v105
	ds_read_b64_tr_b16 v[212:213], v179 offset:50688
	ds_read_b64_tr_b16 v[210:211], v179 offset:49664
	v_exp_f32_e32 v204, v82
	v_exp_f32_e32 v205, v83
	v_exp_f32_e32 v208, v84
	v_exp_f32_e32 v209, v85
	v_exp_f32_e32 v200, v86
	v_exp_f32_e32 v201, v87
	v_exp_f32_e32 v196, v88
	v_exp_f32_e32 v197, v89
	v_cvt_pk_bf16_f32 v102, v190, v191
	v_cvt_pk_bf16_f32 v103, v192, v193
	v_cvt_pk_bf16_f32 v104, v188, v189
	v_cvt_pk_bf16_f32 v105, v186, v187
	v_cvt_pk_bf16_f32 v82, v204, v205
	v_cvt_pk_bf16_f32 v83, v208, v209
	s_waitcnt lgkmcnt(2)
	v_mfma_f32_32x32x16_bf16 v[66:81], v[98:101], v[102:105], v[66:81]
	v_cvt_pk_bf16_f32 v84, v200, v201
	v_cvt_pk_bf16_f32 v85, v196, v197
	v_exp_f32_e32 v206, v106
	v_exp_f32_e32 v207, v107
	v_exp_f32_e32 v202, v108
	v_exp_f32_e32 v203, v109
	v_exp_f32_e32 v198, v110
	s_waitcnt lgkmcnt(0)
	v_mfma_f32_32x32x16_bf16 v[50:65], v[210:213], v[102:105], v[50:65]
	v_exp_f32_e32 v199, v111
	v_exp_f32_e32 v194, v112
	v_exp_f32_e32 v195, v113
	v_exp_f32_e32 v216, v90
	v_exp_f32_e32 v217, v91
	v_exp_f32_e32 v214, v92
	v_exp_f32_e32 v215, v93
	v_mfma_f32_32x32x16_bf16 v[34:49], v[98:101], v[82:85], v[34:49]
	v_cvt_pk_bf16_f32 v86, v206, v207
	v_cvt_pk_bf16_f32 v87, v202, v203
	v_cvt_pk_bf16_f32 v88, v198, v199
	v_cvt_pk_bf16_f32 v89, v194, v195
	v_mfma_f32_32x32x16_bf16 v[18:33], v[210:213], v[82:85], v[18:33]
	ds_read_b64_tr_b16 v[82:83], v179 offset:51200
	ds_read_b64_tr_b16 v[84:85], v179 offset:52224
	ds_read_b64_tr_b16 v[100:101], v179 offset:52736
	ds_read_b64_tr_b16 v[98:99], v179 offset:51712
	v_exp_f32_e32 v212, v94
	v_exp_f32_e32 v213, v95
	v_exp_f32_e32 v210, v96
	v_exp_f32_e32 v211, v97
	s_waitcnt lgkmcnt(2)
	v_mfma_f32_32x32x16_bf16 v[66:81], v[82:85], v[86:89], v[66:81]
	s_waitcnt lgkmcnt(0)
	v_mfma_f32_32x32x16_bf16 v[50:65], v[98:101], v[86:89], v[50:65]
	v_cvt_pk_bf16_f32 v86, v216, v217
	v_cvt_pk_bf16_f32 v87, v214, v215
	v_cvt_pk_bf16_f32 v88, v212, v213
	v_cvt_pk_bf16_f32 v89, v210, v211
	s_nop 1
	v_mfma_f32_32x32x16_bf16 v[34:49], v[82:85], v[86:89], v[34:49]
	v_lshrrev_b32_e32 v82, v163, v227
	v_bfe_i32 v83, v82, 26, 1
	v_bitop3_b32 v96, v16, s28, v83 bitop3:0xe4
	v_bfe_i32 v83, v82, 25, 1
	v_bitop3_b32 v95, v13, s28, v83 bitop3:0xe4
	v_bfe_i32 v83, v82, 24, 1
	v_bitop3_b32 v94, v14, s28, v83 bitop3:0xe4
	v_bfe_i32 v83, v82, 19, 1
	v_bitop3_b32 v93, v11, s28, v83 bitop3:0xe4
	v_bfe_i32 v83, v82, 18, 1
	v_bitop3_b32 v92, v12, s28, v83 bitop3:0xe4
	v_bfe_i32 v83, v82, 17, 1
	v_bitop3_b32 v91, v9, s28, v83 bitop3:0xe4
	v_bfe_i32 v83, v82, 16, 1
	ds_read_b128 v[226:229], v226 offset:4096
	v_bitop3_b32 v90, v10, s28, v83 bitop3:0xe4
	v_bfe_i32 v83, v82, 11, 1
	v_mfma_f32_32x32x16_bf16 v[18:33], v[98:101], v[86:89], v[18:33]
	v_bitop3_b32 v89, v7, s28, v83 bitop3:0xe4
	v_bfe_i32 v83, v82, 10, 1
	v_bitop3_b32 v88, v8, s28, v83 bitop3:0xe4
	v_bfe_i32 v83, v82, 9, 1
	v_bitop3_b32 v87, v5, s28, v83 bitop3:0xe4
	v_bfe_i32 v83, v82, 8, 1
	v_bitop3_b32 v86, v6, s28, v83 bitop3:0xe4
	v_bfe_i32 v83, v82, 3, 1
	v_bfe_i32 v84, v82, 27, 1
	v_bitop3_b32 v85, v3, s28, v83 bitop3:0xe4
	v_bfe_i32 v83, v82, 2, 1
	v_bitop3_b32 v97, v15, s28, v84 bitop3:0xe4
	v_bitop3_b32 v84, v4, s28, v83 bitop3:0xe4
	v_bfe_i32 v83, v82, 1, 1
	v_bfe_i32 v82, v82, 0, 1
	v_bitop3_b32 v83, v1, s28, v83 bitop3:0xe4
	v_bitop3_b32 v82, v2, s28, v82 bitop3:0xe4
	s_waitcnt lgkmcnt(0)
	s_nop 0
	v_mfma_f32_32x32x16_bf16 v[98:113], v[226:229], v[114:117], v[82:97]
	v_mfma_f32_32x32x16_bf16 v[82:97], v[226:229], v[130:133], v[82:97]
	ds_read_b128 v[226:229], v225 offset:4096
	s_waitcnt lgkmcnt(0)
	v_mfma_f32_32x32x16_bf16 v[98:113], v[226:229], v[118:121], v[98:113]
	v_mfma_f32_32x32x16_bf16 v[82:97], v[226:229], v[134:137], v[82:97]
	ds_read_b128 v[224:227], v224 offset:4096
	s_waitcnt lgkmcnt(0)
	v_mfma_f32_32x32x16_bf16 v[98:113], v[224:227], v[122:125], v[98:113]
	v_mfma_f32_32x32x16_bf16 v[82:97], v[224:227], v[138:141], v[82:97]
	ds_read_b128 v[224:227], v223 offset:4096
	s_waitcnt lgkmcnt(0)
	v_mfma_f32_32x32x16_bf16 v[98:113], v[224:227], v[126:129], v[98:113]
	v_mfma_f32_32x32x16_bf16 v[82:97], v[224:227], v[142:145], v[82:97]
	v_add_f32_e64 v240, v190, 0
	v_add_f32_e64 v242, v204, 0
	v_add_f32_e64 v241, v191, 0
	v_add_f32_e64 v243, v205, 0
	v_add_f32_e64 v240, v192, v240
	v_add_f32_e64 v242, v208, v242
	v_add_f32_e64 v241, v193, v241
	v_add_f32_e64 v243, v209, v243
	v_pk_add_f32 v[240:241], v[188:189], v[240:241]
	v_pk_add_f32 v[242:243], v[200:201], v[242:243]
	v_pk_add_f32 v[240:241], v[186:187], v[240:241]
	v_pk_add_f32 v[242:243], v[196:197], v[242:243]
	v_pk_add_f32 v[240:241], v[206:207], v[240:241]
	v_pk_add_f32 v[242:243], v[216:217], v[242:243]
	v_pk_add_f32 v[240:241], v[202:203], v[240:241]
	v_pk_add_f32 v[242:243], v[214:215], v[242:243]
	v_pk_add_f32 v[240:241], v[198:199], v[240:241]
	v_pk_add_f32 v[242:243], v[212:213], v[242:243]
	v_pk_add_f32 v[240:241], v[194:195], v[240:241]
	v_pk_add_f32 v[242:243], v[210:211], v[242:243]
	v_exp_f32_e32 v228, v98
	v_exp_f32_e32 v229, v99
	v_exp_f32_e32 v230, v100
	v_exp_f32_e32 v231, v101
	ds_read_b64_tr_b16 v[98:99], v179 offset:53248
	ds_read_b64_tr_b16 v[100:101], v179 offset:54272
	v_exp_f32_e32 v232, v102
	v_exp_f32_e32 v233, v103
	v_exp_f32_e32 v234, v104
	v_exp_f32_e32 v235, v105
	ds_read_b64_tr_b16 v[226:227], v179 offset:54784
	ds_read_b64_tr_b16 v[224:225], v179 offset:53760
	v_cvt_pk_bf16_f32 v102, v228, v229
	v_cvt_pk_bf16_f32 v103, v230, v231
	v_cvt_pk_bf16_f32 v104, v232, v233
	v_cvt_pk_bf16_f32 v105, v234, v235
	v_exp_f32_e32 v236, v86
	v_exp_f32_e32 v237, v87
	s_waitcnt lgkmcnt(2)
	v_mfma_f32_32x32x16_bf16 v[66:81], v[98:101], v[102:105], v[66:81]
	v_exp_f32_e32 v238, v88
	v_exp_f32_e32 v239, v89
	v_exp_f32_e32 v106, v106
	v_exp_f32_e32 v107, v107
	v_exp_f32_e32 v108, v108
	v_exp_f32_e32 v109, v109
	v_exp_f32_e32 v110, v110
	s_waitcnt lgkmcnt(0)
	v_mfma_f32_32x32x16_bf16 v[50:65], v[224:227], v[102:105], v[50:65]
	v_exp_f32_e32 v102, v82
	v_exp_f32_e32 v103, v83
	v_exp_f32_e32 v104, v84
	v_exp_f32_e32 v105, v85
	v_cvt_pk_bf16_f32 v84, v236, v237
	v_cvt_pk_bf16_f32 v82, v102, v103
	v_cvt_pk_bf16_f32 v85, v238, v239
	v_cvt_pk_bf16_f32 v83, v104, v105
	v_exp_f32_e32 v111, v111
	v_exp_f32_e32 v112, v112
	v_mfma_f32_32x32x16_bf16 v[34:49], v[98:101], v[82:85], v[34:49]
	v_exp_f32_e32 v113, v113
	v_exp_f32_e32 v90, v90
	v_exp_f32_e32 v91, v91
	v_exp_f32_e32 v92, v92
	v_exp_f32_e32 v93, v93
	v_exp_f32_e32 v94, v94
	v_exp_f32_e32 v95, v95
	v_mfma_f32_32x32x16_bf16 v[18:33], v[224:227], v[82:85], v[18:33]
	ds_read_b64_tr_b16 v[82:83], v179 offset:55296
	ds_read_b64_tr_b16 v[84:85], v179 offset:56320
	ds_read_b64_tr_b16 v[100:101], v179 offset:56832
	ds_read_b64_tr_b16 v[98:99], v179 offset:55808
	v_exp_f32_e32 v96, v96
	v_exp_f32_e32 v97, v97
	v_cvt_pk_bf16_f32 v86, v106, v107
	v_cvt_pk_bf16_f32 v87, v108, v109
	v_cvt_pk_bf16_f32 v88, v110, v111
	v_cvt_pk_bf16_f32 v89, v112, v113
	s_waitcnt lgkmcnt(2)
	s_nop 0
	v_mfma_f32_32x32x16_bf16 v[66:81], v[82:85], v[86:89], v[66:81]
	s_waitcnt lgkmcnt(0)
	v_mfma_f32_32x32x16_bf16 v[50:65], v[98:101], v[86:89], v[50:65]
	v_cvt_pk_bf16_f32 v86, v90, v91
	v_cvt_pk_bf16_f32 v87, v92, v93
	v_cvt_pk_bf16_f32 v88, v94, v95
	v_cvt_pk_bf16_f32 v89, v96, v97
	s_nop 1
	v_mfma_f32_32x32x16_bf16 v[34:49], v[82:85], v[86:89], v[34:49]
	v_add_f32_e64 v84, v228, 0
	v_add_f32_e64 v85, v229, 0
	v_pk_add_f32 v[84:85], v[230:231], v[84:85]
	v_pk_add_f32 v[84:85], v[232:233], v[84:85]
	v_mfma_f32_32x32x16_bf16 v[18:33], v[98:101], v[86:89], v[18:33]
	v_add_f32_e64 v88, v102, 0
	v_add_f32_e64 v89, v103, 0
	v_pk_add_f32 v[88:89], v[104:105], v[88:89]
	v_pk_add_f32 v[88:89], v[236:237], v[88:89]
	v_pk_add_f32 v[84:85], v[234:235], v[84:85]
	v_pk_add_f32 v[88:89], v[238:239], v[88:89]
	v_pk_add_f32 v[84:85], v[106:107], v[84:85]
	v_pk_add_f32 v[88:89], v[90:91], v[88:89]
	v_pk_add_f32 v[84:85], v[108:109], v[84:85]
	v_pk_add_f32 v[88:89], v[92:93], v[88:89]
	v_pk_add_f32 v[84:85], v[110:111], v[84:85]
	v_pk_add_f32 v[88:89], v[94:95], v[88:89]
	v_pk_add_f32 v[84:85], v[112:113], v[84:85]
	v_pk_add_f32 v[88:89], v[96:97], v[88:89]
	v_pk_add_f32 v[82:83], v[240:241], v[84:85]
	v_pk_add_f32 v[84:85], v[242:243], v[88:89]
	v_mov_b32_e32 v86, v82
	v_mov_b32_e32 v87, v84
	v_mov_b32_e32 v84, v83
	v_pk_add_f32 v[82:83], v[86:87], v[84:85]
	s_nop 0
	v_pk_add_f32 v[184:185], v[184:185], v[82:83]
	s_cbranch_scc1 .LBB0_2745
.LBB0_2752:
	s_cmp_lg_u32 s35, s0
	s_cbranch_scc0 .Lp13_w0
	s_waitcnt vmcnt(4)
.LBB0_2756:
	s_barrier
	ds_read_b64 v[226:227], v146
	s_lshl_b32 s14, s37, 14
	v_add_u32_e32 v240, s14, v151
	v_add_u32_e32 v240, v240, v153
	ds_read_b128 v[186:189], v240
	s_lshl_b32 s39, s37, 14
	s_cmp_le_u32 s38, s34
	s_cbranch_scc0 .LBB0_2751
	s_add_i32 s14, s39, 0xffffc000
	s_cmp_lg_u32 s37, 0
	s_cselect_b32 s40, s14, 0x8000
	v_lshl_add_u64 v[82:83], v[182:183], 0, s[0:1]
	s_mov_b64 s[14:15], 0x39208000
	s_add_i32 s40, s22, s40
	v_lshl_add_u64 v[84:85], v[82:83], 0, s[14:15]
	s_mov_b32 m0, s40
	s_mov_b64 s[14:15], 0x39208080
	global_load_lds_dwordx4 v[84:85], off
	v_lshl_add_u64 v[82:83], v[82:83], 0, s[14:15]
	s_add_i32 m0, s40, 0x2000
	s_mov_b64 s[14:15], 0x3a208000
	global_load_lds_dwordx4 v[82:83], off
	v_lshl_add_u64 v[82:83], v[172:173], 0, s[0:1]
	v_lshl_add_u64 v[84:85], v[82:83], 0, s[14:15]
	s_add_i32 m0, s40, 0xc000
	v_lshl_add_u64 v[82:83], v[82:83], 0, s[12:13]
	global_load_lds_dwordx4 v[84:85], off
	s_add_i32 m0, s40, 0xe000
	s_nop 0
	global_load_lds_dwordx4 v[82:83], off
	s_branch .LBB0_2751
.Lp13_w0:
	s_waitcnt vmcnt(0)
	s_branch .LBB0_2756
